# pro_a weight-conversion loads: nt -> sc0 sc1 nt (system-scope streaming) on top of v50
# speedup vs baseline: 1.0170x; 1.0002x over previous
.LBB0_14:
	v_add_u32_e32 v28, s33, v71
	v_add_u32_e32 v4, 0x41, v28
	v_ashrrev_i32_e32 v29, 31, v28
	v_ashrrev_i32_e32 v5, 31, v4
	v_lshlrev_b64 v[0:1], 12, v[28:29]
	v_lshlrev_b64 v[4:5], 12, v[4:5]
	v_lshl_add_u64 v[0:1], v[72:73], 0, v[0:1]
	v_lshl_add_u64 v[4:5], v[72:73], 0, v[4:5]
	global_load_dwordx4 v[32:35], v[0:1], off sc0 sc1 nt
	global_load_dwordx4 v[8:11], v[4:5], off sc0 sc1 nt
	v_or_b32_e32 v0, 1, v28
	v_add_u32_e32 v4, 0x42, v28
	v_ashrrev_i32_e32 v1, 31, v0
	v_ashrrev_i32_e32 v5, 31, v4
	v_lshlrev_b64 v[0:1], 12, v[0:1]
	v_lshlrev_b64 v[4:5], 12, v[4:5]
	v_lshl_add_u64 v[0:1], v[72:73], 0, v[0:1]
	v_lshl_add_u64 v[4:5], v[72:73], 0, v[4:5]
	global_load_dwordx4 v[36:39], v[0:1], off sc0 sc1 nt
	global_load_dwordx4 v[16:19], v[4:5], off sc0 sc1 nt
	v_or_b32_e32 v0, 2, v28
	v_add_u32_e32 v4, 0x43, v28
	v_ashrrev_i32_e32 v1, 31, v0
	v_ashrrev_i32_e32 v5, 31, v4
	v_lshlrev_b64 v[0:1], 12, v[0:1]
	v_lshlrev_b64 v[4:5], 12, v[4:5]
	v_lshl_add_u64 v[0:1], v[72:73], 0, v[0:1]
	v_lshl_add_u64 v[4:5], v[72:73], 0, v[4:5]
	global_load_dwordx4 v[44:47], v[0:1], off sc0 sc1 nt
	global_load_dwordx4 v[24:27], v[4:5], off sc0 sc1 nt
	v_or_b32_e32 v0, 3, v28
	v_add_u32_e32 v4, 0x44, v28
	v_ashrrev_i32_e32 v1, 31, v0
	v_ashrrev_i32_e32 v5, 31, v4
	v_lshlrev_b64 v[0:1], 12, v[0:1]
	v_lshlrev_b64 v[4:5], 12, v[4:5]
	v_lshl_add_u64 v[0:1], v[72:73], 0, v[0:1]
	v_lshl_add_u64 v[4:5], v[72:73], 0, v[4:5]
	global_load_dwordx4 v[52:55], v[0:1], off sc0 sc1 nt
	v_add_u32_e32 v12, 0x45, v28
	global_load_dwordx4 v[4:7], v[4:5], off sc0 sc1 nt
	v_or_b32_e32 v0, 4, v28
	v_ashrrev_i32_e32 v1, 31, v0
	v_ashrrev_i32_e32 v13, 31, v12
	v_lshlrev_b64 v[0:1], 12, v[0:1]
	v_lshlrev_b64 v[12:13], 12, v[12:13]
	v_lshl_add_u64 v[0:1], v[72:73], 0, v[0:1]
	v_lshl_add_u64 v[12:13], v[72:73], 0, v[12:13]
	global_load_dwordx4 v[40:43], v[0:1], off sc0 sc1 nt
	v_add_u32_e32 v20, 0x46, v28
	global_load_dwordx4 v[12:15], v[12:13], off sc0 sc1 nt
	v_or_b32_e32 v0, 5, v28
	v_ashrrev_i32_e32 v1, 31, v0
	v_ashrrev_i32_e32 v21, 31, v20
	v_lshlrev_b64 v[0:1], 12, v[0:1]
	v_lshlrev_b64 v[20:21], 12, v[20:21]
	v_lshl_add_u64 v[0:1], v[72:73], 0, v[0:1]
	v_lshl_add_u64 v[20:21], v[72:73], 0, v[20:21]
	global_load_dwordx4 v[48:51], v[0:1], off sc0 sc1 nt
	v_mov_b32_e32 v128, 0
	global_load_dwordx4 v[20:23], v[20:21], off sc0 sc1 nt
	v_or_b32_e32 v0, 6, v28
	v_ashrrev_i32_e32 v1, 31, v0
	v_lshlrev_b64 v[0:1], 12, v[0:1]
	v_lshl_add_u64 v[0:1], v[72:73], 0, v[0:1]
	global_load_dwordx4 v[56:59], v[0:1], off sc0 sc1 nt
	v_or_b32_e32 v0, 7, v28
	v_ashrrev_i32_e32 v1, 31, v0
	v_lshlrev_b64 v[0:1], 12, v[0:1]
	v_lshl_add_u64 v[0:1], v[72:73], 0, v[0:1]
	global_load_dwordx4 v[60:63], v[0:1], off sc0 sc1 nt
	v_add_u32_e32 v0, 64, v28
	v_ashrrev_i32_e32 v1, 31, v0
	v_lshlrev_b64 v[0:1], 12, v[0:1]
	v_lshl_add_u64 v[0:1], v[72:73], 0, v[0:1]
	global_load_dwordx4 v[0:3], v[0:1], off sc0 sc1 nt
	v_add_u32_e32 v28, 0x47, v28
	v_ashrrev_i32_e32 v29, 31, v28
	v_lshlrev_b64 v[28:29], 12, v[28:29]
	v_lshl_add_u64 v[28:29], v[72:73], 0, v[28:29]
	global_load_dwordx4 v[28:31], v[28:29], off sc0 sc1 nt
	v_mov_b32_e32 v129, 0
	s_and_b64 vcc, exec, s[16:17]
	s_mov_b64 s[16:17], 0
	s_waitcnt vmcnt(15)
	v_mul_f32_e32 v32, 0x42000000, v32
	v_mul_f32_e32 v33, 0x42000000, v33
	v_mul_f32_e32 v34, 0x42000000, v34
	v_mul_f32_e32 v35, 0x42000000, v35
	s_waitcnt vmcnt(14)
	v_mul_f32_e32 v8, 0x42000000, v8
	s_waitcnt vmcnt(13)
	v_mul_f32_e32 v36, 0x42000000, v36
	v_cvt_pk_fp8_f32 v128, v32, v36
	s_waitcnt vmcnt(12)
	v_mul_f32_e32 v16, 0x42000000, v16
	s_waitcnt vmcnt(11)
	v_mul_f32_e32 v44, 0x42000000, v44
	s_waitcnt vmcnt(10)
	v_mul_f32_e32 v24, 0x42000000, v24
	s_waitcnt vmcnt(9)
	v_mul_f32_e32 v52, 0x42000000, v52
	v_cvt_pk_fp8_f32 v128, v44, v52 op_sel:[0,0,1]
	s_waitcnt vmcnt(7)
	v_mul_f32_e32 v32, 0x42000000, v40
	s_waitcnt vmcnt(5)
	v_mul_f32_e32 v36, 0x42000000, v48
	v_cvt_pk_fp8_f32 v129, v32, v36
	v_mul_f32_e32 v36, 0x42000000, v37
	v_mov_b32_e32 v32, 0
	v_cvt_pk_fp8_f32 v32, v33, v36
	v_mul_f32_e32 v37, 0x42000000, v45
	v_mul_f32_e32 v36, 0x42000000, v41
	s_waitcnt vmcnt(3)
	v_mul_f32_e32 v40, 0x42000000, v56
	v_mov_b32_e32 v33, 0
	v_mul_f32_e32 v41, 0x42000000, v57
	s_waitcnt vmcnt(2)
	v_mul_f32_e32 v44, 0x42000000, v60
	v_cvt_pk_fp8_f32 v129, v40, v44 op_sel:[0,0,1]
	v_mul_f32_e32 v44, 0x42000000, v53
	v_cvt_pk_fp8_f32 v32, v37, v44 op_sel:[0,0,1]
	v_mul_f32_e32 v37, 0x42000000, v49
	v_cvt_pk_fp8_f32 v33, v36, v37
	v_mul_f32_e32 v37, 0x42000000, v38
	v_mov_b32_e32 v36, 0
	v_cvt_pk_fp8_f32 v36, v34, v37
	v_mul_f32_e32 v44, 0x42000000, v61
	v_cvt_pk_fp8_f32 v33, v41, v44 op_sel:[0,0,1]
	v_mul_f32_e32 v38, 0x42000000, v46
	v_mul_f32_e32 v41, 0x42000000, v54
	v_cvt_pk_fp8_f32 v36, v38, v41 op_sel:[0,0,1]
	v_mul_f32_e32 v34, 0x42000000, v42
	v_mul_f32_e32 v38, 0x42000000, v50
	v_mov_b32_e32 v37, 0
	v_cvt_pk_fp8_f32 v37, v34, v38
	v_mul_f32_e32 v38, 0x42000000, v39
	v_mov_b32_e32 v34, 0
	v_cvt_pk_fp8_f32 v34, v35, v38
	v_mul_f32_e32 v41, 0x42000000, v58
	v_mul_f32_e32 v42, 0x42000000, v62
	v_cvt_pk_fp8_f32 v37, v41, v42 op_sel:[0,0,1]
	v_mul_f32_e32 v39, 0x42000000, v47
	v_mul_f32_e32 v41, 0x42000000, v55
	v_cvt_pk_fp8_f32 v34, v39, v41 op_sel:[0,0,1]
	v_mul_f32_e32 v38, 0x42000000, v43
	v_mul_f32_e32 v39, 0x42000000, v51
	v_mov_b32_e32 v35, 0
	v_cvt_pk_fp8_f32 v35, v38, v39
	s_waitcnt vmcnt(1)
	v_mul_f32_e32 v0, 0x42000000, v0
	v_mov_b32_e32 v38, 0
	v_cvt_pk_fp8_f32 v38, v0, v8
	v_mul_f32_e32 v0, 0x42000000, v4
	v_mul_f32_e32 v4, 0x42000000, v12
	v_mov_b32_e32 v39, 0
	v_cvt_pk_fp8_f32 v39, v0, v4
	v_mul_f32_e32 v1, 0x42000000, v1
	v_mul_f32_e32 v4, 0x42000000, v9
	v_mov_b32_e32 v0, 0
	v_cvt_pk_fp8_f32 v0, v1, v4
	v_mul_f32_e32 v4, 0x42000000, v5
	v_mul_f32_e32 v5, 0x42000000, v13
	v_mov_b32_e32 v1, 0
	v_cvt_pk_fp8_f32 v1, v4, v5
	v_mul_f32_e32 v8, 0x42000000, v20
	s_waitcnt vmcnt(0)
	v_mul_f32_e32 v12, 0x42000000, v28
	v_cvt_pk_fp8_f32 v39, v8, v12 op_sel:[0,0,1]
	v_mul_f32_e32 v8, 0x42000000, v17
	v_mul_f32_e32 v9, 0x42000000, v25
	v_cvt_pk_fp8_f32 v0, v8, v9 op_sel:[0,0,1]
	v_mul_f32_e32 v8, 0x42000000, v21
	v_mul_f32_e32 v9, 0x42000000, v29
	v_cvt_pk_fp8_f32 v1, v8, v9 op_sel:[0,0,1]
	v_add_u32_e32 v40, s33, v125
	v_mul_f32_e32 v4, 0x42000000, v18
	v_mul_f32_e32 v5, 0x42000000, v26
	ds_write2_b64 v40, v[32:33], v[0:1] offset0:34 offset1:42
	v_mul_f32_e32 v1, 0x42000000, v2
	v_mul_f32_e32 v2, 0x42000000, v10
	v_mov_b32_e32 v0, 0
	v_cvt_pk_fp8_f32 v0, v1, v2
	v_mul_f32_e32 v2, 0x42000000, v6
	v_mov_b32_e32 v1, 0
	v_mul_f32_e32 v6, 0x42000000, v30
	v_cvt_pk_fp8_f32 v0, v4, v5 op_sel:[0,0,1]
	v_mul_f32_e32 v4, 0x42000000, v14
	v_cvt_pk_fp8_f32 v1, v2, v4
	v_mul_f32_e32 v5, 0x42000000, v22
	v_mul_f32_e32 v2, 0x42000000, v11
	v_mul_f32_e32 v4, 0x42000000, v27
	v_cvt_pk_fp8_f32 v1, v5, v6 op_sel:[0,0,1]
	v_mul_f32_e32 v41, 0x42000000, v59
	v_mul_f32_e32 v42, 0x42000000, v63
	v_mul_f32_e32 v5, 0x42000000, v31
	ds_write2_b64 v40, v[36:37], v[0:1] offset0:68 offset1:76
	v_mul_f32_e32 v1, 0x42000000, v3
	v_mov_b32_e32 v0, 0
	v_cvt_pk_fp8_f32 v0, v1, v2
	v_mul_f32_e32 v3, 0x42000000, v19
	v_mul_f32_e32 v2, 0x42000000, v7
	v_mov_b32_e32 v1, 0
	v_cvt_pk_fp8_f32 v0, v3, v4 op_sel:[0,0,1]
	v_mul_f32_e32 v3, 0x42000000, v15
	v_cvt_pk_fp8_f32 v1, v2, v3
	v_mul_f32_e32 v4, 0x42000000, v23
	v_cvt_pk_fp8_f32 v35, v41, v42 op_sel:[0,0,1]
	v_cvt_pk_fp8_f32 v38, v16, v24 op_sel:[0,0,1]
	v_cvt_pk_fp8_f32 v1, v4, v5 op_sel:[0,0,1]
	s_movk_i32 s33, 0x80
	ds_write2_b64 v40, v[128:129], v[38:39] offset1:8
	ds_write2_b64 v40, v[34:35], v[0:1] offset0:102 offset1:110
	s_cbranch_vccnz .LBB0_14
	s_add_u32 s14, s18, s14
	s_waitcnt lgkmcnt(0)
	s_barrier
	v_add_u32_e32 v0, v77, v66
	s_addc_u32 s15, s19, s15
	ds_read_b128 v[0:3], v0
	v_add_u32_e32 v4, s2, v76
	s_add_u32 s14, s14, s31
	v_ashrrev_i32_e32 v5, 31, v4
	s_addc_u32 s15, s15, 0
	v_lshlrev_b64 v[4:5], 10, v[4:5]
	v_lshl_add_u64 v[4:5], s[14:15], 0, v[4:5]
	v_lshl_add_u64 v[8:9], v[4:5], 0, v[66:67]
	v_add_u32_e32 v4, v79, v66
	ds_read_b128 v[4:7], v4
	s_waitcnt lgkmcnt(1)
	global_store_dwordx4 v[8:9], v[0:3], off sc1
	s_nop 1
	v_add_u32_e32 v0, s2, v78
	v_ashrrev_i32_e32 v1, 31, v0
	v_lshlrev_b64 v[0:1], 10, v[0:1]
	v_lshl_add_u64 v[0:1], s[14:15], 0, v[0:1]
	v_lshl_add_u64 v[0:1], v[0:1], 0, v[66:67]
	s_waitcnt lgkmcnt(0)
	global_store_dwordx4 v[0:1], v[4:7], off sc1
	v_add_u32_e32 v0, v81, v66
	ds_read_b128 v[0:3], v0
	v_add_u32_e32 v4, s2, v80
	v_ashrrev_i32_e32 v5, 31, v4
	v_lshlrev_b64 v[4:5], 10, v[4:5]
	v_lshl_add_u64 v[4:5], s[14:15], 0, v[4:5]
	v_lshl_add_u64 v[8:9], v[4:5], 0, v[66:67]
	v_add_u32_e32 v4, v83, v66
	ds_read_b128 v[4:7], v4
	s_waitcnt lgkmcnt(1)
	global_store_dwordx4 v[8:9], v[0:3], off sc1
	s_nop 1
	v_add_u32_e32 v0, s2, v82
	v_ashrrev_i32_e32 v1, 31, v0
	v_lshlrev_b64 v[0:1], 10, v[0:1]
	v_lshl_add_u64 v[0:1], s[14:15], 0, v[0:1]
	v_lshl_add_u64 v[0:1], v[0:1], 0, v[66:67]
	s_waitcnt lgkmcnt(0)
	global_store_dwordx4 v[0:1], v[4:7], off sc1
	v_add_u32_e32 v0, v85, v66
	ds_read_b128 v[0:3], v0
	v_add_u32_e32 v4, s2, v84
	v_ashrrev_i32_e32 v5, 31, v4
	v_lshlrev_b64 v[4:5], 10, v[4:5]
	v_lshl_add_u64 v[4:5], s[14:15], 0, v[4:5]
	v_lshl_add_u64 v[8:9], v[4:5], 0, v[66:67]
	v_add_u32_e32 v4, v87, v66
	ds_read_b128 v[4:7], v4
	s_waitcnt lgkmcnt(1)
	global_store_dwordx4 v[8:9], v[0:3], off sc1
	s_nop 1
	v_add_u32_e32 v0, s2, v86
	v_ashrrev_i32_e32 v1, 31, v0
	v_lshlrev_b64 v[0:1], 10, v[0:1]
	v_lshl_add_u64 v[0:1], s[14:15], 0, v[0:1]
	v_lshl_add_u64 v[0:1], v[0:1], 0, v[66:67]
	s_waitcnt lgkmcnt(0)
	global_store_dwordx4 v[0:1], v[4:7], off sc1
	v_add_u32_e32 v0, v89, v66
	ds_read_b128 v[0:3], v0
	v_add_u32_e32 v4, s2, v88
	v_ashrrev_i32_e32 v5, 31, v4
	v_lshlrev_b64 v[4:5], 10, v[4:5]
	v_lshl_add_u64 v[4:5], s[14:15], 0, v[4:5]
	v_lshl_add_u64 v[8:9], v[4:5], 0, v[66:67]
	v_add_u32_e32 v4, v124, v66
	ds_read_b128 v[4:7], v4
	s_waitcnt lgkmcnt(1)
	global_store_dwordx4 v[8:9], v[0:3], off sc1
	s_nop 1
	v_add_u32_e32 v0, s2, v90
	v_ashrrev_i32_e32 v1, 31, v0
	v_lshlrev_b64 v[0:1], 10, v[0:1]
	v_lshl_add_u64 v[0:1], s[14:15], 0, v[0:1]
	v_lshl_add_u64 v[0:1], v[0:1], 0, v[66:67]
	s_waitcnt lgkmcnt(0)
	global_store_dwordx4 v[0:1], v[4:7], off sc1
	s_waitcnt lgkmcnt(0)
	s_barrier

.LBB0_20:
	v_add_u32_e32 v28, s31, v71
	v_add_u32_e32 v4, 0x41, v28
	v_ashrrev_i32_e32 v29, 31, v28
	v_ashrrev_i32_e32 v5, 31, v4
	v_lshlrev_b64 v[0:1], 13, v[28:29]
	v_lshlrev_b64 v[4:5], 13, v[4:5]
	v_lshl_add_u64 v[0:1], v[72:73], 0, v[0:1]
	v_lshl_add_u64 v[4:5], v[72:73], 0, v[4:5]
	global_load_dwordx4 v[32:35], v[0:1], off sc0 sc1 nt
	global_load_dwordx4 v[8:11], v[4:5], off sc0 sc1 nt
	v_or_b32_e32 v0, 1, v28
	v_add_u32_e32 v4, 0x42, v28
	v_ashrrev_i32_e32 v1, 31, v0
	v_ashrrev_i32_e32 v5, 31, v4
	v_lshlrev_b64 v[0:1], 13, v[0:1]
	v_lshlrev_b64 v[4:5], 13, v[4:5]
	v_lshl_add_u64 v[0:1], v[72:73], 0, v[0:1]
	v_lshl_add_u64 v[4:5], v[72:73], 0, v[4:5]
	global_load_dwordx4 v[36:39], v[0:1], off sc0 sc1 nt
	global_load_dwordx4 v[16:19], v[4:5], off sc0 sc1 nt
	v_or_b32_e32 v0, 2, v28
	v_add_u32_e32 v4, 0x43, v28
	v_ashrrev_i32_e32 v1, 31, v0
	v_ashrrev_i32_e32 v5, 31, v4
	v_lshlrev_b64 v[0:1], 13, v[0:1]
	v_lshlrev_b64 v[4:5], 13, v[4:5]
	v_lshl_add_u64 v[0:1], v[72:73], 0, v[0:1]
	v_lshl_add_u64 v[4:5], v[72:73], 0, v[4:5]
	global_load_dwordx4 v[44:47], v[0:1], off sc0 sc1 nt
	global_load_dwordx4 v[24:27], v[4:5], off sc0 sc1 nt
	v_or_b32_e32 v0, 3, v28
	v_add_u32_e32 v4, 0x44, v28
	v_ashrrev_i32_e32 v1, 31, v0
	v_ashrrev_i32_e32 v5, 31, v4
	v_lshlrev_b64 v[0:1], 13, v[0:1]
	v_lshlrev_b64 v[4:5], 13, v[4:5]
	v_lshl_add_u64 v[0:1], v[72:73], 0, v[0:1]
	v_lshl_add_u64 v[4:5], v[72:73], 0, v[4:5]
	global_load_dwordx4 v[52:55], v[0:1], off sc0 sc1 nt
	v_add_u32_e32 v12, 0x45, v28
	global_load_dwordx4 v[4:7], v[4:5], off sc0 sc1 nt
	v_or_b32_e32 v0, 4, v28
	v_ashrrev_i32_e32 v1, 31, v0
	v_ashrrev_i32_e32 v13, 31, v12
	v_lshlrev_b64 v[0:1], 13, v[0:1]
	v_lshlrev_b64 v[12:13], 13, v[12:13]
	v_lshl_add_u64 v[0:1], v[72:73], 0, v[0:1]
	v_lshl_add_u64 v[12:13], v[72:73], 0, v[12:13]
	global_load_dwordx4 v[40:43], v[0:1], off sc0 sc1 nt
	v_add_u32_e32 v20, 0x46, v28
	global_load_dwordx4 v[12:15], v[12:13], off sc0 sc1 nt
	v_or_b32_e32 v0, 5, v28
	v_ashrrev_i32_e32 v1, 31, v0
	v_ashrrev_i32_e32 v21, 31, v20
	v_lshlrev_b64 v[0:1], 13, v[0:1]
	v_lshlrev_b64 v[20:21], 13, v[20:21]
	v_lshl_add_u64 v[0:1], v[72:73], 0, v[0:1]
	v_lshl_add_u64 v[20:21], v[72:73], 0, v[20:21]
	global_load_dwordx4 v[48:51], v[0:1], off sc0 sc1 nt
	v_mov_b32_e32 v128, 0
	global_load_dwordx4 v[20:23], v[20:21], off sc0 sc1 nt
	v_or_b32_e32 v0, 6, v28
	v_ashrrev_i32_e32 v1, 31, v0
	v_lshlrev_b64 v[0:1], 13, v[0:1]
	v_lshl_add_u64 v[0:1], v[72:73], 0, v[0:1]
	global_load_dwordx4 v[56:59], v[0:1], off sc0 sc1 nt
	v_or_b32_e32 v0, 7, v28
	v_ashrrev_i32_e32 v1, 31, v0
	v_lshlrev_b64 v[0:1], 13, v[0:1]
	v_lshl_add_u64 v[0:1], v[72:73], 0, v[0:1]
	global_load_dwordx4 v[60:63], v[0:1], off sc0 sc1 nt
	v_add_u32_e32 v0, 64, v28
	v_ashrrev_i32_e32 v1, 31, v0
	v_lshlrev_b64 v[0:1], 13, v[0:1]
	v_lshl_add_u64 v[0:1], v[72:73], 0, v[0:1]
	global_load_dwordx4 v[0:3], v[0:1], off sc0 sc1 nt
	v_add_u32_e32 v28, 0x47, v28
	v_ashrrev_i32_e32 v29, 31, v28
	v_lshlrev_b64 v[28:29], 13, v[28:29]
	v_lshl_add_u64 v[28:29], v[72:73], 0, v[28:29]
	global_load_dwordx4 v[28:31], v[28:29], off sc0 sc1 nt
	v_mov_b32_e32 v129, 0
	s_and_b64 vcc, exec, s[14:15]
	s_mov_b64 s[14:15], 0
	s_waitcnt vmcnt(15)
	v_mul_f32_e32 v32, 0x42000000, v32
	v_mul_f32_e32 v33, 0x42000000, v33
	v_mul_f32_e32 v34, 0x42000000, v34
	v_mul_f32_e32 v35, 0x42000000, v35
	s_waitcnt vmcnt(14)
	v_mul_f32_e32 v8, 0x42000000, v8
	s_waitcnt vmcnt(13)
	v_mul_f32_e32 v36, 0x42000000, v36
	v_cvt_pk_fp8_f32 v128, v32, v36
	s_waitcnt vmcnt(12)
	v_mul_f32_e32 v16, 0x42000000, v16
	s_waitcnt vmcnt(11)
	v_mul_f32_e32 v44, 0x42000000, v44
	s_waitcnt vmcnt(10)
	v_mul_f32_e32 v24, 0x42000000, v24
	s_waitcnt vmcnt(9)
	v_mul_f32_e32 v52, 0x42000000, v52
	v_cvt_pk_fp8_f32 v128, v44, v52 op_sel:[0,0,1]
	s_waitcnt vmcnt(7)
	v_mul_f32_e32 v32, 0x42000000, v40
	s_waitcnt vmcnt(5)
	v_mul_f32_e32 v36, 0x42000000, v48
	v_cvt_pk_fp8_f32 v129, v32, v36
	v_mul_f32_e32 v36, 0x42000000, v37
	v_mov_b32_e32 v32, 0
	v_cvt_pk_fp8_f32 v32, v33, v36
	v_mul_f32_e32 v37, 0x42000000, v45
	v_mul_f32_e32 v36, 0x42000000, v41
	s_waitcnt vmcnt(3)
	v_mul_f32_e32 v40, 0x42000000, v56
	v_mov_b32_e32 v33, 0
	v_mul_f32_e32 v41, 0x42000000, v57
	s_waitcnt vmcnt(2)
	v_mul_f32_e32 v44, 0x42000000, v60
	v_cvt_pk_fp8_f32 v129, v40, v44 op_sel:[0,0,1]
	v_mul_f32_e32 v44, 0x42000000, v53
	v_cvt_pk_fp8_f32 v32, v37, v44 op_sel:[0,0,1]
	v_mul_f32_e32 v37, 0x42000000, v49
	v_cvt_pk_fp8_f32 v33, v36, v37
	v_mul_f32_e32 v37, 0x42000000, v38
	v_mov_b32_e32 v36, 0
	v_cvt_pk_fp8_f32 v36, v34, v37
	v_mul_f32_e32 v44, 0x42000000, v61
	v_cvt_pk_fp8_f32 v33, v41, v44 op_sel:[0,0,1]
	v_mul_f32_e32 v38, 0x42000000, v46
	v_mul_f32_e32 v41, 0x42000000, v54
	v_cvt_pk_fp8_f32 v36, v38, v41 op_sel:[0,0,1]
	v_mul_f32_e32 v34, 0x42000000, v42
	v_mul_f32_e32 v38, 0x42000000, v50
	v_mov_b32_e32 v37, 0
	v_cvt_pk_fp8_f32 v37, v34, v38
	v_mul_f32_e32 v38, 0x42000000, v39
	v_mov_b32_e32 v34, 0
	v_cvt_pk_fp8_f32 v34, v35, v38
	v_mul_f32_e32 v41, 0x42000000, v58
	v_mul_f32_e32 v42, 0x42000000, v62
	v_cvt_pk_fp8_f32 v37, v41, v42 op_sel:[0,0,1]
	v_mul_f32_e32 v39, 0x42000000, v47
	v_mul_f32_e32 v41, 0x42000000, v55
	v_cvt_pk_fp8_f32 v34, v39, v41 op_sel:[0,0,1]
	v_mul_f32_e32 v38, 0x42000000, v43
	v_mul_f32_e32 v39, 0x42000000, v51
	v_mov_b32_e32 v35, 0
	v_cvt_pk_fp8_f32 v35, v38, v39
	s_waitcnt vmcnt(1)
	v_mul_f32_e32 v0, 0x42000000, v0
	v_mov_b32_e32 v38, 0
	v_cvt_pk_fp8_f32 v38, v0, v8
	v_mul_f32_e32 v0, 0x42000000, v4
	v_mul_f32_e32 v4, 0x42000000, v12
	v_mov_b32_e32 v39, 0
	v_cvt_pk_fp8_f32 v39, v0, v4
	v_mul_f32_e32 v1, 0x42000000, v1
	v_mul_f32_e32 v4, 0x42000000, v9
	v_mov_b32_e32 v0, 0
	v_cvt_pk_fp8_f32 v0, v1, v4
	v_mul_f32_e32 v4, 0x42000000, v5
	v_mul_f32_e32 v5, 0x42000000, v13
	v_mov_b32_e32 v1, 0
	v_cvt_pk_fp8_f32 v1, v4, v5
	v_mul_f32_e32 v8, 0x42000000, v20
	s_waitcnt vmcnt(0)
	v_mul_f32_e32 v12, 0x42000000, v28
	v_cvt_pk_fp8_f32 v39, v8, v12 op_sel:[0,0,1]
	v_mul_f32_e32 v8, 0x42000000, v17
	v_mul_f32_e32 v9, 0x42000000, v25
	v_cvt_pk_fp8_f32 v0, v8, v9 op_sel:[0,0,1]
	v_mul_f32_e32 v8, 0x42000000, v21
	v_mul_f32_e32 v9, 0x42000000, v29
	v_cvt_pk_fp8_f32 v1, v8, v9 op_sel:[0,0,1]
	v_add_u32_e32 v40, s31, v125
	v_mul_f32_e32 v4, 0x42000000, v18
	v_mul_f32_e32 v5, 0x42000000, v26
	ds_write2_b64 v40, v[32:33], v[0:1] offset0:34 offset1:42
	v_mul_f32_e32 v1, 0x42000000, v2
	v_mul_f32_e32 v2, 0x42000000, v10
	v_mov_b32_e32 v0, 0
	v_cvt_pk_fp8_f32 v0, v1, v2
	v_mul_f32_e32 v2, 0x42000000, v6
	v_mov_b32_e32 v1, 0
	v_mul_f32_e32 v6, 0x42000000, v30
	v_cvt_pk_fp8_f32 v0, v4, v5 op_sel:[0,0,1]
	v_mul_f32_e32 v4, 0x42000000, v14
	v_cvt_pk_fp8_f32 v1, v2, v4
	v_mul_f32_e32 v5, 0x42000000, v22
	v_mul_f32_e32 v2, 0x42000000, v11
	v_mul_f32_e32 v4, 0x42000000, v27
	v_cvt_pk_fp8_f32 v1, v5, v6 op_sel:[0,0,1]
	v_mul_f32_e32 v41, 0x42000000, v59
	v_mul_f32_e32 v42, 0x42000000, v63
	v_mul_f32_e32 v5, 0x42000000, v31
	ds_write2_b64 v40, v[36:37], v[0:1] offset0:68 offset1:76
	v_mul_f32_e32 v1, 0x42000000, v3
	v_mov_b32_e32 v0, 0
	v_cvt_pk_fp8_f32 v0, v1, v2
	v_mul_f32_e32 v3, 0x42000000, v19
	v_mul_f32_e32 v2, 0x42000000, v7
	v_mov_b32_e32 v1, 0
	v_cvt_pk_fp8_f32 v0, v3, v4 op_sel:[0,0,1]
	v_mul_f32_e32 v3, 0x42000000, v15
	v_cvt_pk_fp8_f32 v1, v2, v3
	v_mul_f32_e32 v4, 0x42000000, v23
	v_cvt_pk_fp8_f32 v35, v41, v42 op_sel:[0,0,1]
	v_cvt_pk_fp8_f32 v38, v16, v24 op_sel:[0,0,1]
	v_cvt_pk_fp8_f32 v1, v4, v5 op_sel:[0,0,1]
	s_movk_i32 s31, 0x80
	ds_write2_b64 v40, v[128:129], v[38:39] offset1:8
	ds_write2_b64 v40, v[34:35], v[0:1] offset0:102 offset1:110
	s_cbranch_vccnz .LBB0_20
	s_lshl_b64 s[14:15], s[2:3], 21
	s_add_u32 s2, s21, s14
	s_waitcnt lgkmcnt(0)
	s_barrier
	v_add_u32_e32 v0, v77, v66
	s_addc_u32 s15, s22, s15
	ds_read_b128 v[0:3], v0
	v_add_u32_e32 v4, s16, v76
	s_add_u32 s14, s2, s17
	v_ashrrev_i32_e32 v5, 31, v4
	s_addc_u32 s15, s15, 0
	v_lshlrev_b64 v[4:5], 10, v[4:5]
	v_lshl_add_u64 v[4:5], s[14:15], 0, v[4:5]
	v_lshl_add_u64 v[8:9], v[4:5], 0, v[66:67]
	v_add_u32_e32 v4, v79, v66
	ds_read_b128 v[4:7], v4
	s_waitcnt lgkmcnt(1)
	global_store_dwordx4 v[8:9], v[0:3], off sc1
	s_nop 1
	v_add_u32_e32 v0, s16, v78
	v_ashrrev_i32_e32 v1, 31, v0
	v_lshlrev_b64 v[0:1], 10, v[0:1]
	v_lshl_add_u64 v[0:1], s[14:15], 0, v[0:1]
	v_lshl_add_u64 v[0:1], v[0:1], 0, v[66:67]
	s_waitcnt lgkmcnt(0)
	global_store_dwordx4 v[0:1], v[4:7], off sc1
	v_add_u32_e32 v0, v81, v66
	ds_read_b128 v[0:3], v0
	v_add_u32_e32 v4, s16, v80
	v_ashrrev_i32_e32 v5, 31, v4
	v_lshlrev_b64 v[4:5], 10, v[4:5]
	v_lshl_add_u64 v[4:5], s[14:15], 0, v[4:5]
	v_lshl_add_u64 v[8:9], v[4:5], 0, v[66:67]
	v_add_u32_e32 v4, v83, v66
	ds_read_b128 v[4:7], v4
	s_waitcnt lgkmcnt(1)
	global_store_dwordx4 v[8:9], v[0:3], off sc1
	s_nop 1
	v_add_u32_e32 v0, s16, v82
	v_ashrrev_i32_e32 v1, 31, v0
	v_lshlrev_b64 v[0:1], 10, v[0:1]
	v_lshl_add_u64 v[0:1], s[14:15], 0, v[0:1]
	v_lshl_add_u64 v[0:1], v[0:1], 0, v[66:67]
	s_waitcnt lgkmcnt(0)
	global_store_dwordx4 v[0:1], v[4:7], off sc1
	v_add_u32_e32 v0, v85, v66
	ds_read_b128 v[0:3], v0
	v_add_u32_e32 v4, s16, v84
	v_ashrrev_i32_e32 v5, 31, v4
	v_lshlrev_b64 v[4:5], 10, v[4:5]
	v_lshl_add_u64 v[4:5], s[14:15], 0, v[4:5]
	v_lshl_add_u64 v[8:9], v[4:5], 0, v[66:67]
	v_add_u32_e32 v4, v87, v66
	ds_read_b128 v[4:7], v4
	s_waitcnt lgkmcnt(1)
	global_store_dwordx4 v[8:9], v[0:3], off sc1
	s_nop 1
	v_add_u32_e32 v0, s16, v86
	v_ashrrev_i32_e32 v1, 31, v0
	v_lshlrev_b64 v[0:1], 10, v[0:1]
	v_lshl_add_u64 v[0:1], s[14:15], 0, v[0:1]
	v_lshl_add_u64 v[0:1], v[0:1], 0, v[66:67]
	s_waitcnt lgkmcnt(0)
	global_store_dwordx4 v[0:1], v[4:7], off sc1
	v_add_u32_e32 v0, v89, v66
	ds_read_b128 v[0:3], v0
	v_add_u32_e32 v4, s16, v88
	v_ashrrev_i32_e32 v5, 31, v4
	v_lshlrev_b64 v[4:5], 10, v[4:5]
	v_lshl_add_u64 v[4:5], s[14:15], 0, v[4:5]
	v_lshl_add_u64 v[8:9], v[4:5], 0, v[66:67]
	v_add_u32_e32 v4, v124, v66
	ds_read_b128 v[4:7], v4
	s_waitcnt lgkmcnt(1)
	global_store_dwordx4 v[8:9], v[0:3], off sc1
	s_nop 1
	v_add_u32_e32 v0, s16, v90
	v_ashrrev_i32_e32 v1, 31, v0
	v_lshlrev_b64 v[0:1], 10, v[0:1]
	v_lshl_add_u64 v[0:1], s[14:15], 0, v[0:1]
	v_lshl_add_u64 v[0:1], v[0:1], 0, v[66:67]
	s_waitcnt lgkmcnt(0)
	global_store_dwordx4 v[0:1], v[4:7], off sc1
	s_waitcnt lgkmcnt(0)
	s_barrier

.LBB0_25:
	v_lshl_add_u32 v32, s33, 6, v26
	v_or_b32_e32 v4, 1, v32
	v_ashrrev_i32_e32 v33, 31, v32
	v_ashrrev_i32_e32 v5, 31, v4
	s_or_b32 s34, s33, 1
	v_lshlrev_b64 v[0:1], 12, v[32:33]
	v_lshlrev_b64 v[4:5], 12, v[4:5]
	v_or_b32_e32 v8, 2, v32
	v_or_b32_e32 v12, 3, v32
	v_or_b32_e32 v16, 4, v32
	v_or_b32_e32 v20, 5, v32
	v_or_b32_e32 v28, 6, v32
	v_or_b32_e32 v32, 7, v32
	v_lshl_add_u32 v72, s34, 6, v26
	v_lshl_add_u64 v[0:1], v[24:25], 0, v[0:1]
	v_lshl_add_u64 v[4:5], v[24:25], 0, v[4:5]
	v_ashrrev_i32_e32 v9, 31, v8
	v_ashrrev_i32_e32 v13, 31, v12
	v_ashrrev_i32_e32 v17, 31, v16
	v_ashrrev_i32_e32 v21, 31, v20
	v_ashrrev_i32_e32 v29, 31, v28
	v_ashrrev_i32_e32 v33, 31, v32
	v_ashrrev_i32_e32 v73, 31, v72
	global_load_dwordx4 v[0:3], v[0:1], off sc0 sc1 nt
	v_lshlrev_b64 v[8:9], 12, v[8:9]
	global_load_dwordx4 v[4:7], v[4:5], off sc0 sc1 nt
	v_lshlrev_b64 v[12:13], 12, v[12:13]
	v_lshlrev_b64 v[16:17], 12, v[16:17]
	v_lshlrev_b64 v[20:21], 12, v[20:21]
	v_lshlrev_b64 v[28:29], 12, v[28:29]
	v_lshlrev_b64 v[32:33], 12, v[32:33]
	v_lshlrev_b64 v[36:37], 12, v[72:73]
	v_or_b32_e32 v40, 1, v72
	v_or_b32_e32 v44, 2, v72
	v_or_b32_e32 v48, 3, v72
	v_or_b32_e32 v52, 4, v72
	v_or_b32_e32 v56, 5, v72
	v_or_b32_e32 v60, 6, v72
	v_or_b32_e32 v72, 7, v72
	v_lshl_add_u64 v[8:9], v[24:25], 0, v[8:9]
	v_lshl_add_u64 v[12:13], v[24:25], 0, v[12:13]
	v_lshl_add_u64 v[16:17], v[24:25], 0, v[16:17]
	v_lshl_add_u64 v[20:21], v[24:25], 0, v[20:21]
	v_lshl_add_u64 v[28:29], v[24:25], 0, v[28:29]
	v_lshl_add_u64 v[32:33], v[24:25], 0, v[32:33]
	v_ashrrev_i32_e32 v41, 31, v40
	v_ashrrev_i32_e32 v45, 31, v44
	v_ashrrev_i32_e32 v49, 31, v48
	v_ashrrev_i32_e32 v53, 31, v52
	v_ashrrev_i32_e32 v57, 31, v56
	v_ashrrev_i32_e32 v61, 31, v60
	v_ashrrev_i32_e32 v73, 31, v72
	s_waitcnt vmcnt(0)
	v_cvt_pk_bf16_f32 v132, v0, v4
	v_lshl_add_u32 v4, s33, 7, v123
	global_load_dwordx4 v[8:11], v[8:9], off sc0 sc1 nt
	v_lshlrev_b64 v[40:41], 12, v[40:41]
	global_load_dwordx4 v[12:15], v[12:13], off sc0 sc1 nt
	v_lshlrev_b64 v[44:45], 12, v[44:45]
	global_load_dwordx4 v[16:19], v[16:17], off sc0 sc1 nt
	v_lshlrev_b64 v[48:49], 12, v[48:49]
	global_load_dwordx4 v[20:23], v[20:21], off sc0 sc1 nt
	v_lshlrev_b64 v[52:53], 12, v[52:53]
	global_load_dwordx4 v[28:31], v[28:29], off sc0 sc1 nt
	v_lshlrev_b64 v[56:57], 12, v[56:57]
	global_load_dwordx4 v[32:35], v[32:33], off sc0 sc1 nt
	v_lshlrev_b64 v[60:61], 12, v[60:61]
	v_lshlrev_b64 v[72:73], 12, v[72:73]
	s_waitcnt vmcnt(4)
	v_cvt_pk_bf16_f32 v133, v8, v12
	s_waitcnt vmcnt(2)
	v_cvt_pk_bf16_f32 v134, v16, v20
	s_waitcnt vmcnt(0)
	v_cvt_pk_bf16_f32 v135, v28, v32
	ds_write_b128 v4, v[132:135]
	v_cvt_pk_bf16_f32 v132, v1, v5
	v_lshl_add_u64 v[36:37], v[24:25], 0, v[36:37]
	v_lshl_add_u64 v[40:41], v[24:25], 0, v[40:41]
	v_lshl_add_u64 v[44:45], v[24:25], 0, v[44:45]
	v_lshl_add_u64 v[48:49], v[24:25], 0, v[48:49]
	v_lshl_add_u64 v[52:53], v[24:25], 0, v[52:53]
	v_lshl_add_u64 v[56:57], v[24:25], 0, v[56:57]
	v_lshl_add_u64 v[60:61], v[24:25], 0, v[60:61]
	v_lshl_add_u64 v[72:73], v[24:25], 0, v[72:73]
	v_cvt_pk_bf16_f32 v133, v9, v13
	v_cvt_pk_bf16_f32 v134, v17, v21
	v_cvt_pk_bf16_f32 v135, v29, v33
	ds_write_b128 v4, v[132:135] offset:528
	v_cvt_pk_bf16_f32 v132, v2, v6
	v_cvt_pk_bf16_f32 v0, v3, v7
	v_cvt_pk_bf16_f32 v1, v11, v15
	v_cvt_pk_bf16_f32 v2, v19, v23
	v_cvt_pk_bf16_f32 v3, v31, v35
	global_load_dwordx4 v[36:39], v[36:37], off sc0 sc1 nt
	v_cvt_pk_bf16_f32 v133, v10, v14
	global_load_dwordx4 v[40:43], v[40:41], off sc0 sc1 nt
	v_cvt_pk_bf16_f32 v134, v18, v22
	global_load_dwordx4 v[44:47], v[44:45], off sc0 sc1 nt
	v_cvt_pk_bf16_f32 v135, v30, v34
	global_load_dwordx4 v[48:51], v[48:49], off sc0 sc1 nt
	ds_write_b128 v4, v[132:135] offset:1056
	global_load_dwordx4 v[52:55], v[52:53], off sc0 sc1 nt
	ds_write_b128 v4, v[0:3] offset:1584
	global_load_dwordx4 v[56:59], v[56:57], off sc0 sc1 nt
	s_waitcnt vmcnt(4)
	v_cvt_pk_bf16_f32 v0, v36, v40
	global_load_dwordx4 v[60:63], v[60:61], off sc0 sc1 nt
	s_waitcnt vmcnt(3)
	v_cvt_pk_bf16_f32 v1, v44, v48
	global_load_dwordx4 v[128:131], v[72:73], off sc0 sc1 nt
	s_waitcnt vmcnt(2)
	v_cvt_pk_bf16_f32 v2, v52, v56
	s_waitcnt vmcnt(0)
	v_cvt_pk_bf16_f32 v3, v60, v128
	v_lshl_add_u32 v4, s34, 7, v123
	ds_write_b128 v4, v[0:3]
	v_cvt_pk_bf16_f32 v0, v37, v41
	v_cvt_pk_bf16_f32 v1, v45, v49
	v_cvt_pk_bf16_f32 v2, v53, v57
	v_cvt_pk_bf16_f32 v3, v61, v129
	ds_write_b128 v4, v[0:3] offset:528
	v_cvt_pk_bf16_f32 v0, v38, v42
	v_cvt_pk_bf16_f32 v1, v46, v50
	v_cvt_pk_bf16_f32 v2, v54, v58
	v_cvt_pk_bf16_f32 v3, v62, v130
	s_and_b64 vcc, exec, s[16:17]
	s_mov_b64 s[16:17], 0
	s_mov_b32 s33, 2
	ds_write_b128 v4, v[0:3] offset:1056
	v_cvt_pk_bf16_f32 v0, v39, v43
	v_cvt_pk_bf16_f32 v1, v47, v51
	v_cvt_pk_bf16_f32 v2, v55, v59
	v_cvt_pk_bf16_f32 v3, v63, v131
	ds_write_b128 v4, v[0:3] offset:1584
	s_cbranch_vccnz .LBB0_25
	s_lshl_b64 s[14:15], s[14:15], 1
	s_add_u32 s14, s23, s14
	s_waitcnt lgkmcnt(0)
	s_barrier
	s_addc_u32 s15, s24, s15
	s_lshl_b32 s16, s31, 1
	ds_read_b128 v[0:3], v92
	v_add_u32_e32 v4, s2, v91
	s_add_u32 s14, s14, s16
	v_ashrrev_i32_e32 v5, 31, v4
	s_addc_u32 s15, s15, 0
	v_lshlrev_b64 v[4:5], 11, v[4:5]
	v_lshl_add_u64 v[4:5], s[14:15], 0, v[4:5]
	v_mov_b32_e32 v71, v69
	v_lshl_add_u64 v[8:9], v[4:5], 0, v[70:71]
	ds_read_b128 v[4:7], v94
	s_waitcnt lgkmcnt(1)
	global_store_dwordx4 v[8:9], v[0:3], off sc1
	s_nop 1
	v_add_u32_e32 v0, s2, v93
	v_ashrrev_i32_e32 v1, 31, v0
	v_lshlrev_b64 v[0:1], 11, v[0:1]
	v_lshl_add_u64 v[0:1], s[14:15], 0, v[0:1]
	v_lshl_add_u64 v[0:1], v[0:1], 0, v[70:71]
	s_waitcnt lgkmcnt(0)
	global_store_dwordx4 v[0:1], v[4:7], off sc1
	ds_read_b128 v[0:3], v96
	s_nop 0
	v_add_u32_e32 v4, s2, v95
	v_ashrrev_i32_e32 v5, 31, v4
	v_lshlrev_b64 v[4:5], 11, v[4:5]
	v_lshl_add_u64 v[4:5], s[14:15], 0, v[4:5]
	v_lshl_add_u64 v[8:9], v[4:5], 0, v[70:71]
	ds_read_b128 v[4:7], v98
	s_waitcnt lgkmcnt(1)
	global_store_dwordx4 v[8:9], v[0:3], off sc1
	s_nop 1
	v_add_u32_e32 v0, s2, v97
	v_ashrrev_i32_e32 v1, 31, v0
	v_lshlrev_b64 v[0:1], 11, v[0:1]
	v_lshl_add_u64 v[0:1], s[14:15], 0, v[0:1]
	v_lshl_add_u64 v[0:1], v[0:1], 0, v[70:71]
	s_waitcnt lgkmcnt(0)
	global_store_dwordx4 v[0:1], v[4:7], off sc1
	ds_read_b128 v[0:3], v100
	s_nop 0
	v_add_u32_e32 v4, s2, v99
	v_ashrrev_i32_e32 v5, 31, v4
	v_lshlrev_b64 v[4:5], 11, v[4:5]
	v_lshl_add_u64 v[4:5], s[14:15], 0, v[4:5]
	v_lshl_add_u64 v[8:9], v[4:5], 0, v[70:71]
	ds_read_b128 v[4:7], v102
	s_waitcnt lgkmcnt(1)
	global_store_dwordx4 v[8:9], v[0:3], off sc1
	s_nop 1
	v_add_u32_e32 v0, s2, v101
	v_ashrrev_i32_e32 v1, 31, v0
	v_lshlrev_b64 v[0:1], 11, v[0:1]
	v_lshl_add_u64 v[0:1], s[14:15], 0, v[0:1]
	v_lshl_add_u64 v[0:1], v[0:1], 0, v[70:71]
	s_waitcnt lgkmcnt(0)
	global_store_dwordx4 v[0:1], v[4:7], off sc1
	ds_read_b128 v[0:3], v104
	s_nop 0
	v_add_u32_e32 v4, s2, v103
	v_ashrrev_i32_e32 v5, 31, v4
	v_lshlrev_b64 v[4:5], 11, v[4:5]
	v_lshl_add_u64 v[4:5], s[14:15], 0, v[4:5]
	v_lshl_add_u64 v[8:9], v[4:5], 0, v[70:71]
	ds_read_b128 v[4:7], v106
	s_waitcnt lgkmcnt(1)
	global_store_dwordx4 v[8:9], v[0:3], off sc1
	s_nop 1
	v_add_u32_e32 v0, s2, v105
	v_ashrrev_i32_e32 v1, 31, v0
	v_lshlrev_b64 v[0:1], 11, v[0:1]
	v_lshl_add_u64 v[0:1], s[14:15], 0, v[0:1]
	v_lshl_add_u64 v[0:1], v[0:1], 0, v[70:71]
	s_waitcnt lgkmcnt(0)
	global_store_dwordx4 v[0:1], v[4:7], off sc1
	ds_read_b128 v[0:3], v108
	s_nop 0
	v_add_u32_e32 v4, s2, v107
	v_ashrrev_i32_e32 v5, 31, v4
	v_lshlrev_b64 v[4:5], 11, v[4:5]
	v_lshl_add_u64 v[4:5], s[14:15], 0, v[4:5]
	v_lshl_add_u64 v[8:9], v[4:5], 0, v[70:71]
	ds_read_b128 v[4:7], v110
	s_waitcnt lgkmcnt(1)
	global_store_dwordx4 v[8:9], v[0:3], off sc1
	s_nop 1
	v_add_u32_e32 v0, s2, v109
	v_ashrrev_i32_e32 v1, 31, v0
	v_lshlrev_b64 v[0:1], 11, v[0:1]
	v_lshl_add_u64 v[0:1], s[14:15], 0, v[0:1]
	v_lshl_add_u64 v[0:1], v[0:1], 0, v[70:71]
	s_waitcnt lgkmcnt(0)
	global_store_dwordx4 v[0:1], v[4:7], off sc1
	ds_read_b128 v[0:3], v112
	s_nop 0
	v_add_u32_e32 v4, s2, v111
	v_ashrrev_i32_e32 v5, 31, v4
	v_lshlrev_b64 v[4:5], 11, v[4:5]
	v_lshl_add_u64 v[4:5], s[14:15], 0, v[4:5]
	v_lshl_add_u64 v[8:9], v[4:5], 0, v[70:71]
	ds_read_b128 v[4:7], v114
	s_waitcnt lgkmcnt(1)
	global_store_dwordx4 v[8:9], v[0:3], off sc1
	s_nop 1
	v_add_u32_e32 v0, s2, v113
	v_ashrrev_i32_e32 v1, 31, v0
	v_lshlrev_b64 v[0:1], 11, v[0:1]
	v_lshl_add_u64 v[0:1], s[14:15], 0, v[0:1]
	v_lshl_add_u64 v[0:1], v[0:1], 0, v[70:71]
	s_waitcnt lgkmcnt(0)
	global_store_dwordx4 v[0:1], v[4:7], off sc1
	ds_read_b128 v[0:3], v116
	s_nop 0
	v_add_u32_e32 v4, s2, v115
	v_ashrrev_i32_e32 v5, 31, v4
	v_lshlrev_b64 v[4:5], 11, v[4:5]
	v_lshl_add_u64 v[4:5], s[14:15], 0, v[4:5]
	v_lshl_add_u64 v[8:9], v[4:5], 0, v[70:71]
	ds_read_b128 v[4:7], v118
	s_waitcnt lgkmcnt(1)
	global_store_dwordx4 v[8:9], v[0:3], off sc1
	s_nop 1
	v_add_u32_e32 v0, s2, v117
	v_ashrrev_i32_e32 v1, 31, v0
	v_lshlrev_b64 v[0:1], 11, v[0:1]
	v_lshl_add_u64 v[0:1], s[14:15], 0, v[0:1]
	v_lshl_add_u64 v[0:1], v[0:1], 0, v[70:71]
	s_waitcnt lgkmcnt(0)
	global_store_dwordx4 v[0:1], v[4:7], off sc1
	ds_read_b128 v[0:3], v120
	s_nop 0
	v_add_u32_e32 v4, s2, v119
	v_ashrrev_i32_e32 v5, 31, v4
	v_lshlrev_b64 v[4:5], 11, v[4:5]
	v_lshl_add_u64 v[4:5], s[14:15], 0, v[4:5]
	v_lshl_add_u64 v[8:9], v[4:5], 0, v[70:71]
	ds_read_b128 v[4:7], v122
	s_waitcnt lgkmcnt(1)
	global_store_dwordx4 v[8:9], v[0:3], off sc1
	s_nop 1
	v_add_u32_e32 v0, s2, v121
	v_ashrrev_i32_e32 v1, 31, v0
	v_lshlrev_b64 v[0:1], 11, v[0:1]
	v_lshl_add_u64 v[0:1], s[14:15], 0, v[0:1]
	v_lshl_add_u64 v[0:1], v[0:1], 0, v[70:71]
	s_waitcnt lgkmcnt(0)
	global_store_dwordx4 v[0:1], v[4:7], off sc1
	s_waitcnt lgkmcnt(0)
	s_barrier

.LBB0_30:
	v_add_u32_e32 v3, s31, v2
	v_mad_i64_i32 v[4:5], s[34:35], v3, s29, v[0:1]
	v_or_b32_e32 v8, 1, v3
	v_or_b32_e32 v9, 2, v3
	v_or_b32_e32 v10, 3, v3
	v_or_b32_e32 v11, 4, v3
	v_or_b32_e32 v12, 5, v3
	v_or_b32_e32 v13, 6, v3
	v_or_b32_e32 v14, 7, v3
	v_add_u32_e32 v15, 64, v3
	v_add_u32_e32 v16, 0x41, v3
	v_add_u32_e32 v17, 0x42, v3
	v_add_u32_e32 v18, 0x43, v3
	v_add_u32_e32 v19, 0x44, v3
	v_add_u32_e32 v26, 0x45, v3
	v_add_u32_e32 v27, 0x46, v3
	v_add_u32_e32 v3, 0x47, v3
	global_load_dwordx4 v[4:7], v[4:5], off sc0 sc1 nt
	v_mad_i64_i32 v[20:21], s[34:35], v8, s29, v[0:1]
	v_mad_i64_i32 v[22:23], s[34:35], v9, s29, v[0:1]
	v_mad_i64_i32 v[24:25], s[34:35], v10, s29, v[0:1]
	v_mad_i64_i32 v[28:29], s[34:35], v11, s29, v[0:1]
	v_mad_i64_i32 v[30:31], s[34:35], v12, s29, v[0:1]
	v_mad_i64_i32 v[32:33], s[34:35], v13, s29, v[0:1]
	v_mad_i64_i32 v[34:35], s[34:35], v14, s29, v[0:1]
	v_mad_i64_i32 v[36:37], s[34:35], v15, s29, v[0:1]
	v_mad_i64_i32 v[40:41], s[34:35], v16, s29, v[0:1]
	v_mad_i64_i32 v[44:45], s[34:35], v17, s29, v[0:1]
	v_mad_i64_i32 v[48:49], s[34:35], v18, s29, v[0:1]
	v_mad_i64_i32 v[52:53], s[34:35], v19, s29, v[0:1]
	v_mad_i64_i32 v[56:57], s[34:35], v26, s29, v[0:1]
	v_mad_i64_i32 v[60:61], s[34:35], v27, s29, v[0:1]
	v_mad_i64_i32 v[128:129], s[34:35], v3, s29, v[0:1]
	global_load_dwordx4 v[8:11], v[20:21], off sc0 sc1 nt
	global_load_dwordx4 v[12:15], v[22:23], off sc0 sc1 nt
	global_load_dwordx4 v[16:19], v[24:25], off sc0 sc1 nt
	s_nop 0
	global_load_dwordx4 v[20:23], v[28:29], off sc0 sc1 nt
	global_load_dwordx4 v[24:27], v[30:31], off sc0 sc1 nt
	s_nop 0
	global_load_dwordx4 v[28:31], v[32:33], off sc0 sc1 nt
	s_nop 0
	global_load_dwordx4 v[32:35], v[34:35], off sc0 sc1 nt
	s_nop 0
	global_load_dwordx4 v[36:39], v[36:37], off sc0 sc1 nt
	s_nop 0
	global_load_dwordx4 v[40:43], v[40:41], off sc0 sc1 nt
	s_nop 0
	global_load_dwordx4 v[44:47], v[44:45], off sc0 sc1 nt
	s_nop 0
	global_load_dwordx4 v[48:51], v[48:49], off sc0 sc1 nt
	s_nop 0
	global_load_dwordx4 v[52:55], v[52:53], off sc0 sc1 nt
	s_nop 0
	global_load_dwordx4 v[56:59], v[56:57], off sc0 sc1 nt
	s_nop 0
	global_load_dwordx4 v[60:63], v[60:61], off sc0 sc1 nt
	s_nop 0
	global_load_dwordx4 v[128:131], v[128:129], off sc0 sc1 nt
	v_mov_b32_e32 v72, 0
	v_mov_b32_e32 v73, 0
	v_mov_b32_e32 v138, 0
	v_mov_b32_e32 v139, 0
	v_mov_b32_e32 v132, 0
	v_mov_b32_e32 v133, 0
	v_mov_b32_e32 v140, 0
	v_mov_b32_e32 v141, 0
	v_mov_b32_e32 v134, 0
	v_mov_b32_e32 v135, 0
	v_mov_b32_e32 v142, 0
	v_mov_b32_e32 v143, 0
	v_mov_b32_e32 v136, 0
	v_mov_b32_e32 v137, 0
	v_mov_b32_e32 v144, 0
	v_mov_b32_e32 v145, 0
	v_add_u32_e32 v68, s31, v125
	s_movk_i32 s31, 0x80
	s_and_b64 vcc, exec, s[14:15]
	s_mov_b64 s[14:15], 0
	s_waitcnt vmcnt(15)
	v_mul_f32_e32 v3, 0x42000000, v4
	v_mul_f32_e32 v4, 0x42000000, v5
	v_mul_f32_e32 v5, 0x42000000, v6
	v_mul_f32_e32 v6, 0x42000000, v7
	s_waitcnt vmcnt(14)
	v_mul_f32_e32 v7, 0x42000000, v8
	v_mul_f32_e32 v8, 0x42000000, v9
	v_mul_f32_e32 v9, 0x42000000, v10
	v_mul_f32_e32 v10, 0x42000000, v11
	s_waitcnt vmcnt(13)
	v_mul_f32_e32 v11, 0x42000000, v12
	v_mul_f32_e32 v12, 0x42000000, v13
	v_mul_f32_e32 v13, 0x42000000, v14
	v_mul_f32_e32 v14, 0x42000000, v15
	s_waitcnt vmcnt(12)
	v_mul_f32_e32 v15, 0x42000000, v16
	v_mul_f32_e32 v16, 0x42000000, v17
	v_mul_f32_e32 v17, 0x42000000, v18
	v_mul_f32_e32 v18, 0x42000000, v19
	s_waitcnt vmcnt(11)
	v_mul_f32_e32 v19, 0x42000000, v20
	v_mul_f32_e32 v20, 0x42000000, v21
	v_mul_f32_e32 v21, 0x42000000, v22
	v_mul_f32_e32 v22, 0x42000000, v23
	s_waitcnt vmcnt(10)
	v_mul_f32_e32 v23, 0x42000000, v24
	v_mul_f32_e32 v24, 0x42000000, v25
	v_mul_f32_e32 v25, 0x42000000, v26
	v_mul_f32_e32 v26, 0x42000000, v27
	s_waitcnt vmcnt(9)
	v_mul_f32_e32 v27, 0x42000000, v28
	v_mul_f32_e32 v28, 0x42000000, v29
	v_mul_f32_e32 v29, 0x42000000, v30
	v_mul_f32_e32 v30, 0x42000000, v31
	s_waitcnt vmcnt(8)
	v_mul_f32_e32 v31, 0x42000000, v32
	v_mul_f32_e32 v32, 0x42000000, v33
	v_mul_f32_e32 v33, 0x42000000, v34
	v_mul_f32_e32 v34, 0x42000000, v35
	s_waitcnt vmcnt(7)
	v_mul_f32_e32 v35, 0x42000000, v36
	v_mul_f32_e32 v36, 0x42000000, v37
	v_mul_f32_e32 v37, 0x42000000, v38
	v_mul_f32_e32 v38, 0x42000000, v39
	s_waitcnt vmcnt(6)
	v_mul_f32_e32 v39, 0x42000000, v40
	v_mul_f32_e32 v40, 0x42000000, v41
	v_mul_f32_e32 v41, 0x42000000, v42
	v_mul_f32_e32 v42, 0x42000000, v43
	s_waitcnt vmcnt(5)
	v_mul_f32_e32 v43, 0x42000000, v44
	v_mul_f32_e32 v44, 0x42000000, v45
	v_mul_f32_e32 v45, 0x42000000, v46
	v_mul_f32_e32 v46, 0x42000000, v47
	s_waitcnt vmcnt(4)
	v_mul_f32_e32 v47, 0x42000000, v48
	v_mul_f32_e32 v48, 0x42000000, v49
	v_mul_f32_e32 v49, 0x42000000, v50
	v_mul_f32_e32 v50, 0x42000000, v51
	s_waitcnt vmcnt(3)
	v_mul_f32_e32 v51, 0x42000000, v52
	v_mul_f32_e32 v52, 0x42000000, v53
	v_mul_f32_e32 v53, 0x42000000, v54
	v_mul_f32_e32 v54, 0x42000000, v55
	s_waitcnt vmcnt(2)
	v_mul_f32_e32 v55, 0x42000000, v56
	v_mul_f32_e32 v56, 0x42000000, v57
	v_cvt_pk_fp8_f32 v72, v3, v7
	v_cvt_pk_fp8_f32 v73, v19, v23
	v_cvt_pk_fp8_f32 v138, v35, v39
	v_cvt_pk_fp8_f32 v139, v51, v55
	v_mul_f32_e32 v57, 0x42000000, v58
	v_cvt_pk_fp8_f32 v132, v4, v8
	v_cvt_pk_fp8_f32 v133, v20, v24
	v_cvt_pk_fp8_f32 v140, v36, v40
	v_cvt_pk_fp8_f32 v141, v52, v56
	v_mul_f32_e32 v58, 0x42000000, v59
	v_cvt_pk_fp8_f32 v134, v5, v9
	v_cvt_pk_fp8_f32 v135, v21, v25
	v_cvt_pk_fp8_f32 v142, v37, v41
	v_cvt_pk_fp8_f32 v143, v53, v57
	s_waitcnt vmcnt(1)
	v_mul_f32_e32 v59, 0x42000000, v60
	v_mul_f32_e32 v60, 0x42000000, v61
	v_mul_f32_e32 v61, 0x42000000, v62
	v_mul_f32_e32 v62, 0x42000000, v63
	s_waitcnt vmcnt(0)
	v_mul_f32_e32 v63, 0x42000000, v128
	v_cvt_pk_fp8_f32 v136, v6, v10
	v_cvt_pk_fp8_f32 v137, v22, v26
	v_cvt_pk_fp8_f32 v144, v38, v42
	v_cvt_pk_fp8_f32 v145, v54, v58
	v_mul_f32_e32 v71, 0x42000000, v129
	v_cvt_pk_fp8_f32 v72, v11, v15 op_sel:[0,0,1]
	v_cvt_pk_fp8_f32 v73, v27, v31 op_sel:[0,0,1]
	v_cvt_pk_fp8_f32 v138, v43, v47 op_sel:[0,0,1]
	v_cvt_pk_fp8_f32 v139, v59, v63 op_sel:[0,0,1]
	v_mul_f32_e32 v127, 0x42000000, v130
	v_cvt_pk_fp8_f32 v132, v12, v16 op_sel:[0,0,1]
	v_cvt_pk_fp8_f32 v133, v28, v32 op_sel:[0,0,1]
	v_cvt_pk_fp8_f32 v140, v44, v48 op_sel:[0,0,1]
	v_cvt_pk_fp8_f32 v141, v60, v71 op_sel:[0,0,1]
	v_mul_f32_e32 v128, 0x42000000, v131
	v_cvt_pk_fp8_f32 v134, v13, v17 op_sel:[0,0,1]
	v_cvt_pk_fp8_f32 v135, v29, v33 op_sel:[0,0,1]
	v_cvt_pk_fp8_f32 v142, v45, v49 op_sel:[0,0,1]
	v_cvt_pk_fp8_f32 v143, v61, v127 op_sel:[0,0,1]
	v_cvt_pk_fp8_f32 v136, v14, v18 op_sel:[0,0,1]
	v_cvt_pk_fp8_f32 v137, v30, v34 op_sel:[0,0,1]
	v_cvt_pk_fp8_f32 v144, v46, v50 op_sel:[0,0,1]
	v_cvt_pk_fp8_f32 v145, v62, v128 op_sel:[0,0,1]
	ds_write2_b64 v68, v[72:73], v[138:139] offset1:8
	ds_write2_b64 v68, v[132:133], v[140:141] offset0:34 offset1:42
	ds_write2_b64 v68, v[134:135], v[142:143] offset0:68 offset1:76
	ds_write2_b64 v68, v[136:137], v[144:145] offset0:102 offset1:110
	s_cbranch_vccnz .LBB0_30
	s_mul_i32 s15, s16, 0x280000
	s_mul_hi_i32 s14, s16, 0x280000
	s_add_u32 s15, s25, s15
	s_waitcnt lgkmcnt(0)
	s_barrier
	v_add_u32_e32 v0, v77, v66
	s_addc_u32 s16, s27, s14
	s_ashr_i32 s31, s17, 31
	ds_read_b128 v[0:3], v0
	v_add_u32_e32 v4, s2, v76
	s_add_u32 s14, s15, s17
	v_ashrrev_i32_e32 v5, 31, v4
	s_addc_u32 s15, s16, s31
	v_lshlrev_b64 v[4:5], 10, v[4:5]
	v_lshl_add_u64 v[4:5], s[14:15], 0, v[4:5]
	v_lshl_add_u64 v[8:9], v[4:5], 0, v[66:67]
	v_add_u32_e32 v4, v79, v66
	ds_read_b128 v[4:7], v4
	s_waitcnt lgkmcnt(1)
	global_store_dwordx4 v[8:9], v[0:3], off sc1
	s_nop 1
	v_add_u32_e32 v0, s2, v78
	v_ashrrev_i32_e32 v1, 31, v0
	v_lshlrev_b64 v[0:1], 10, v[0:1]
	v_lshl_add_u64 v[0:1], s[14:15], 0, v[0:1]
	v_lshl_add_u64 v[0:1], v[0:1], 0, v[66:67]
	s_waitcnt lgkmcnt(0)
	global_store_dwordx4 v[0:1], v[4:7], off sc1
	v_add_u32_e32 v0, v81, v66
	ds_read_b128 v[0:3], v0
	v_add_u32_e32 v4, s2, v80
	v_ashrrev_i32_e32 v5, 31, v4
	v_lshlrev_b64 v[4:5], 10, v[4:5]
	v_lshl_add_u64 v[4:5], s[14:15], 0, v[4:5]
	v_lshl_add_u64 v[8:9], v[4:5], 0, v[66:67]
	v_add_u32_e32 v4, v83, v66
	ds_read_b128 v[4:7], v4
	s_waitcnt lgkmcnt(1)
	global_store_dwordx4 v[8:9], v[0:3], off sc1
	s_nop 1
	v_add_u32_e32 v0, s2, v82
	v_ashrrev_i32_e32 v1, 31, v0
	v_lshlrev_b64 v[0:1], 10, v[0:1]
	v_lshl_add_u64 v[0:1], s[14:15], 0, v[0:1]
	v_lshl_add_u64 v[0:1], v[0:1], 0, v[66:67]
	s_waitcnt lgkmcnt(0)
	global_store_dwordx4 v[0:1], v[4:7], off sc1
	v_add_u32_e32 v0, v85, v66
	ds_read_b128 v[0:3], v0
	v_add_u32_e32 v4, s2, v84
	v_ashrrev_i32_e32 v5, 31, v4
	v_lshlrev_b64 v[4:5], 10, v[4:5]
	v_lshl_add_u64 v[4:5], s[14:15], 0, v[4:5]
	v_lshl_add_u64 v[8:9], v[4:5], 0, v[66:67]
	v_add_u32_e32 v4, v87, v66
	ds_read_b128 v[4:7], v4
	s_waitcnt lgkmcnt(1)
	global_store_dwordx4 v[8:9], v[0:3], off sc1
	s_nop 1
	v_add_u32_e32 v0, s2, v86
	v_ashrrev_i32_e32 v1, 31, v0
	v_lshlrev_b64 v[0:1], 10, v[0:1]
	v_lshl_add_u64 v[0:1], s[14:15], 0, v[0:1]
	v_lshl_add_u64 v[0:1], v[0:1], 0, v[66:67]
	s_waitcnt lgkmcnt(0)
	global_store_dwordx4 v[0:1], v[4:7], off sc1
	v_add_u32_e32 v0, v89, v66
	ds_read_b128 v[0:3], v0
	v_add_u32_e32 v4, s2, v88
	v_ashrrev_i32_e32 v5, 31, v4
	v_lshlrev_b64 v[4:5], 10, v[4:5]
	v_lshl_add_u64 v[4:5], s[14:15], 0, v[4:5]
	v_lshl_add_u64 v[8:9], v[4:5], 0, v[66:67]
	v_add_u32_e32 v4, v124, v66
	ds_read_b128 v[4:7], v4
	s_waitcnt lgkmcnt(1)
	global_store_dwordx4 v[8:9], v[0:3], off sc1
	s_nop 1
	v_add_u32_e32 v0, s2, v90
	v_ashrrev_i32_e32 v1, 31, v0
	v_lshlrev_b64 v[0:1], 10, v[0:1]
	v_lshl_add_u64 v[0:1], s[14:15], 0, v[0:1]
	v_lshl_add_u64 v[0:1], v[0:1], 0, v[66:67]
	s_waitcnt lgkmcnt(0)
	global_store_dwordx4 v[0:1], v[4:7], off sc1
	s_waitcnt lgkmcnt(0)
	s_barrier
	s_branch .LBB0_8
